# GEMM unit decode: the division by the row-group height (always 4) is a shift and a mask instead of the v_rcp + readfirstlane + correction sequence, in all five GEMM phases
# baseline (speedup 1.0000x reference)
.LBB0_186:
	s_add_i32 s56, s56, 1
	s_mul_i32 s2, s56, s57
	s_mul_hi_u32 s3, s56, s46
	s_add_i32 s3, s3, s2
	s_mul_i32 s2, s56, s46
	s_add_u32 s22, s2, s30
	s_addc_u32 s23, s3, s58
	v_mov_b64_e32 v[0:1], 0x1a00
	v_cmp_lt_i64_e64 s[2:3], s[22:23], v[0:1]
	v_mov_b64_e32 v[0:1], 0x19ff
	v_cmp_gt_i64_e32 vcc, s[22:23], v[0:1]
	s_cbranch_vccnz .LBB0_188
	s_ashr_i32 s5, s22, 31
	s_lshr_b32 s5, s5, 29
	s_add_i32 s5, s22, s5
	s_ashr_i32 s7, s5, 3
	s_and_b32 s5, s5, -8
	s_sub_i32 s5, s22, s5
	s_cmp_lt_i32 s5, 0
	s_movk_i32 s18, 0x341
	s_cselect_b32 s18, s18, 0x340
	s_mul_i32 s5, s5, s18
	s_add_i32 s5, s5, s7
	s_mul_hi_i32 s7, s5, 0x4ec4ec4f
	s_lshr_b32 s18, s7, 31
	s_ashr_i32 s7, s7, 6
	s_add_i32 s7, s7, s18
	s_lshl_b32 s19, s7, 2
	s_sub_i32 s18, 0x80, s19
	s_mulk_i32 s7, 0xd0
	s_sub_i32 s5, s5, s7
	s_lshr_b32 s18, s5, 2
	s_and_b32 s5, s5, 3
	s_add_i32 s20, s19, s5

.LBB0_676:
	s_ashr_i32 s2, s12, 3
	s_add_i32 s2, s20, s2
	s_ashr_i32 s3, s2, 31
	s_lshr_b32 s3, s3, 27
	s_add_i32 s3, s2, s3
	s_ashr_i32 s12, s3, 5
	s_lshl_b32 s12, s12, 2
	s_sub_i32 s13, 0x80, s12
	s_andn2_b32 s3, s3, 31
	s_sub_i32 s2, s2, s3
	s_lshr_b32 s51, s2, 2
	s_and_b32 s2, s2, 3
	s_add_i32 s52, s12, s2

.LBB0_749:
	s_ashr_i32 s4, s6, 3
	s_add_i32 s4, s10, s4
	s_ashr_i32 s5, s4, 31
	s_lshr_b32 s5, s5, 27
	s_add_i32 s5, s4, s5
	s_ashr_i32 s6, s5, 5
	s_lshl_b32 s6, s6, 2
	s_sub_i32 s7, 0x80, s6
	s_andn2_b32 s5, s5, 31
	s_sub_i32 s5, s4, s5
	s_lshr_b32 s4, s5, 2
	s_and_b32 s5, s5, 3
	s_add_i32 s6, s6, s5

.LBB0_853:
	s_add_i32 s52, s52, 1
	s_mul_i32 s2, s52, s51
	s_mul_hi_u32 s3, s52, s42
	s_add_i32 s3, s3, s2
	s_mul_i32 s2, s52, s42
	s_add_u32 s12, s2, s24
	s_addc_u32 s13, s3, s29
	v_mov_b64_e32 v[0:1], 0x1600
	v_cmp_lt_i64_e64 s[2:3], s[12:13], v[0:1]
	v_mov_b64_e32 v[0:1], 0x15ff
	v_cmp_gt_i64_e32 vcc, s[12:13], v[0:1]
	s_cbranch_vccnz .LBB0_855
	s_ashr_i32 s8, s12, 31
	s_lshr_b32 s8, s8, 29
	s_add_i32 s8, s12, s8
	s_ashr_i32 s9, s8, 3
	s_and_b32 s8, s8, -8
	s_sub_i32 s8, s12, s8
	s_cmp_lt_i32 s8, 0
	s_movk_i32 s10, 0x2c1
	s_cselect_b32 s10, s10, 0x2c0
	s_mul_i32 s8, s8, s10
	s_add_i32 s8, s8, s9
	s_mul_hi_i32 s9, s8, 0x2e8ba2e9
	s_lshr_b32 s10, s9, 31
	s_ashr_i32 s9, s9, 5
	s_add_i32 s9, s9, s10
	s_lshl_b32 s10, s9, 2
	s_sub_i32 s11, 0x80, s10
	s_mulk_i32 s9, 0xb0
	s_sub_i32 s9, s8, s9
	s_lshr_b32 s8, s9, 2
	s_and_b32 s9, s9, 3
	s_add_i32 s10, s10, s9

.LBB0_921:
	s_ashr_i32 s6, s12, 3
	s_add_i32 s6, s14, s6
	s_ashr_i32 s7, s6, 31
	s_lshr_b32 s7, s7, 27
	s_add_i32 s7, s6, s7
	s_ashr_i32 s12, s7, 5
	s_lshl_b32 s12, s12, 2
	s_sub_i32 s13, 0x80, s12
	s_andn2_b32 s7, s7, 31
	s_sub_i32 s6, s6, s7
	s_lshr_b32 s46, s6, 2
	s_and_b32 s6, s6, 3
	s_add_i32 s47, s12, s6
